# v75 + retention rope block: v-tile conversion and its 4 LDS tile writes moved to the front of the block (fewer LDS writes draining before the chunk barrier)
# speedup vs baseline: 1.0071x; 1.0071x over previous
; #define LAS __attribute__((address_space(3)))
; #define LDS_BARRIER() do { asm volatile("s_waitcnt lgkmcnt(0)" ::: "memory"); __builtin_amdgcn_s_barrier(); asm volatile("" ::: "memory"); } while (0)
; template <int NET> __device__ __forceinline__ void ret_item(Ctx& F, int item) {
;     ...
;     for (int n = 0; n < 16; ++n) {
;         const int t0 = b * SEQ + n * 128;
;         RET_LOAD(n + 1 < 16 ? n + 1 : 15);
;         LDS_BARRIER();
;         f32x4 sacc[8];
; #pragma unroll
;         for (int mt = 0; mt < 8; ++mt) sacc[mt] = (f32x4){0.f, 0.f, 0.f, 0.f};
; #pragma unroll
;         for (int ks = 0; ks < 4; ++ks) { const bf16x8 bq = *(const LAS bf16x8*)(qL + (16 * w + fr) * LP + 32 * ks + 8 * fq);
; #pragma unroll
;             for (int mt = 0; mt < 8; ++mt) { const bf16x8 ak = *(const LAS bf16x8*)(kL + (16 * mt + fr) * LP + 32 * ks + 8 * fq); sacc[mt] = __builtin_amdgcn_mfma_f32_16x16x32_bf16(ak, bq, sacc[mt], 0, 0, 0); } }
.LBB0_314:
	s_add_i32 s74, s33, 0x80
	s_cmpk_eq_i32 s33, 0x780
	s_cselect_b32 s0, s33, s74
	v_add_u32_e32 v18, s0, v112
	v_mov_b64_e32 v[20:21], s[88:89]
	v_ashrrev_i32_e32 v19, 31, v18
	v_mad_i64_i32 v[20:21], s[0:1], v18, s91, v[20:21]
	v_lshlrev_b64 v[42:43], 8, v[18:19]
	v_lshl_add_u64 v[18:19], v[20:21], 0, v[106:107]
	global_load_dwordx4 v[26:29], v[18:19], off offset:16
	global_load_dwordx4 v[50:53], v[18:19], off
	global_load_dwordx4 v[30:33], v[18:19], off offset:144
	global_load_dwordx4 v[54:57], v[18:19], off offset:128
	global_load_dwordx4 v[34:37], v[18:19], off offset:2064
	global_load_dwordx4 v[58:61], v[18:19], off offset:2048
	global_load_dwordx4 v[38:41], v[18:19], off offset:2192
	global_load_dwordx4 v[62:65], v[18:19], off offset:2176
	v_lshl_add_u64 v[18:19], s[80:81], 1, v[20:21]
	v_lshl_add_u64 v[18:19], v[18:19], 0, v[106:107]
	v_lshl_add_u64 v[20:21], v[18:19], 0, s[78:79]
	v_add_co_u32_e64 v18, s[0:1], s92, v18
	v_lshl_add_u64 v[70:71], v[108:109], 0, v[42:43]
	s_nop 0
	v_addc_co_u32_e64 v19, s[0:1], 0, v19, s[0:1]
	global_load_dwordx4 v[22:25], v[18:19], off
	s_nop 0
	global_load_dwordx4 v[18:21], v[20:21], off offset:16
	s_nop 0
	global_load_dwordx4 v[42:45], v[70:71], off offset:48
	global_load_dwordx4 v[46:49], v[70:71], off offset:32
	global_load_dwordx4 v[66:69], v[70:71], off offset:16
	s_nop 0
	global_load_dwordx4 v[70:73], v[70:71], off
	s_waitcnt lgkmcnt(0)
	s_barrier
	ds_read_b128 v[74:77], v163
	ds_read_b128 v[78:81], v187 offset:34816
	ds_read_b128 v[82:85], v187 offset:39168
	ds_read_b128 v[86:89], v187 offset:43520
	ds_read_b128 v[90:93], v187 offset:47872
	ds_read_b128 v[94:97], v187 offset:52224
	ds_read_b128 v[98:101], v187 offset:56576
	ds_read_b128 v[102:105], v187 offset:60928
	ds_read_b128 v[232:235], v187 offset:65280
	s_waitcnt lgkmcnt(7)
	v_mfma_f32_16x16x32_bf16 v[78:81], v[78:81], v[74:77], 0
	v_add_u32_e32 v115, 0x1200, v166
	v_add_u32_e32 v130, 0x2400, v166
	v_add_u32_e32 v131, 0x3600, v166
	s_waitcnt lgkmcnt(6)
	v_mfma_f32_16x16x32_bf16 v[82:85], v[82:85], v[74:77], 0
	v_add_u32_e32 v132, 0x900, v166
	v_add_u32_e32 v133, 0x1b00, v166
	v_add_u32_e32 v248, 0x2d00, v166
	s_waitcnt lgkmcnt(5)
	v_mfma_f32_16x16x32_bf16 v[86:89], v[86:89], v[74:77], 0
	v_add_u32_e32 v249, 0x3f00, v166
	v_add_u32_e32 v124, s33, v111
	v_ashrrev_i32_e32 v125, 31, v124
	s_waitcnt lgkmcnt(4)
	v_mfma_f32_16x16x32_bf16 v[90:93], v[90:93], v[74:77], 0
	v_lshlrev_b64 v[124:125], 12, v[124:125]
	v_lshl_add_u64 v[124:125], v[120:121], 0, v[124:125]
	v_pk_mul_f32 v[10:11], v[122:123], v[10:11]
	s_waitcnt lgkmcnt(3)
	v_mfma_f32_16x16x32_bf16 v[94:97], v[94:97], v[74:77], 0
	v_mul_f32_e64 v14, v122, v14
	v_mul_f32_e64 v15, v123, v15
	v_pk_mul_f32 v[6:7], v[122:123], v[6:7]
	v_pk_mul_f32 v[2:3], v[122:123], v[2:3]
	s_waitcnt lgkmcnt(2)
	v_mfma_f32_16x16x32_bf16 v[98:101], v[98:101], v[74:77], 0
	s_cmpk_lg_i32 s74, 0x800
	s_mov_b32 s33, s74
	s_waitcnt lgkmcnt(1)
	v_mfma_f32_16x16x32_bf16 v[102:105], v[102:105], v[74:77], 0
	s_waitcnt lgkmcnt(0)
	v_mfma_f32_16x16x32_bf16 v[74:77], v[232:235], v[74:77], 0
	ds_read_b128 v[232:235], v163 offset:64
	ds_read_b128 v[236:239], v187 offset:34880
	s_waitcnt lgkmcnt(0)
	v_mfma_f32_16x16x32_bf16 v[78:81], v[236:239], v[232:235], v[78:81]
	ds_read_b128 v[236:239], v187 offset:39232
	s_waitcnt lgkmcnt(0)
	v_mfma_f32_16x16x32_bf16 v[82:85], v[236:239], v[232:235], v[82:85]
	ds_read_b128 v[236:239], v187 offset:43584
	s_waitcnt lgkmcnt(0)
	v_mfma_f32_16x16x32_bf16 v[86:89], v[236:239], v[232:235], v[86:89]
	ds_read_b128 v[236:239], v187 offset:47936
	s_waitcnt lgkmcnt(0)
	v_mfma_f32_16x16x32_bf16 v[90:93], v[236:239], v[232:235], v[90:93]
	ds_read_b128 v[236:239], v187 offset:52288
	s_waitcnt lgkmcnt(0)
	v_mfma_f32_16x16x32_bf16 v[94:97], v[236:239], v[232:235], v[94:97]
	ds_read_b128 v[236:239], v187 offset:56640
	s_waitcnt lgkmcnt(0)
	v_mfma_f32_16x16x32_bf16 v[98:101], v[236:239], v[232:235], v[98:101]
	ds_read_b128 v[236:239], v187 offset:60992
	s_waitcnt lgkmcnt(0)
	v_mfma_f32_16x16x32_bf16 v[102:105], v[236:239], v[232:235], v[102:105]
	ds_read_b128 v[236:239], v187 offset:65344
	s_waitcnt lgkmcnt(0)
	v_mfma_f32_16x16x32_bf16 v[74:77], v[236:239], v[232:235], v[74:77]
	ds_read_b128 v[232:235], v163 offset:128
	ds_read_b128 v[236:239], v187 offset:34944
	s_waitcnt lgkmcnt(0)
	v_mfma_f32_16x16x32_bf16 v[78:81], v[236:239], v[232:235], v[78:81]
	ds_read_b128 v[236:239], v187 offset:39296
	s_waitcnt lgkmcnt(0)
	v_mfma_f32_16x16x32_bf16 v[82:85], v[236:239], v[232:235], v[82:85]
	ds_read_b128 v[236:239], v187 offset:43648
	s_waitcnt lgkmcnt(0)
	v_mfma_f32_16x16x32_bf16 v[86:89], v[236:239], v[232:235], v[86:89]
	ds_read_b128 v[236:239], v187 offset:48000
	s_waitcnt lgkmcnt(0)
	v_mfma_f32_16x16x32_bf16 v[90:93], v[236:239], v[232:235], v[90:93]
	ds_read_b128 v[236:239], v187 offset:52352
	s_waitcnt lgkmcnt(0)
	v_mfma_f32_16x16x32_bf16 v[94:97], v[236:239], v[232:235], v[94:97]
	ds_read_b128 v[236:239], v187 offset:56704
	s_waitcnt lgkmcnt(0)
	v_mfma_f32_16x16x32_bf16 v[98:101], v[236:239], v[232:235], v[98:101]
	ds_read_b128 v[236:239], v187 offset:61056
	s_waitcnt lgkmcnt(0)
	v_mfma_f32_16x16x32_bf16 v[102:105], v[236:239], v[232:235], v[102:105]
	ds_read_b128 v[236:239], v187 offset:65408
	s_waitcnt lgkmcnt(0)
	v_mfma_f32_16x16x32_bf16 v[74:77], v[236:239], v[232:235], v[74:77]
	ds_read_b128 v[232:235], v163 offset:192
	ds_read_b128 v[236:239], v187 offset:35008
	s_waitcnt lgkmcnt(0)
	v_mfma_f32_16x16x32_bf16 v[78:81], v[236:239], v[232:235], v[78:81]
	ds_read_b128 v[236:239], v187 offset:39360
	s_waitcnt lgkmcnt(0)
; #define LAS __attribute__((address_space(3)))
; __device__ __forceinline__ unsigned pk2(float lo, float hi) { unsigned r; asm volatile("v_cvt_pk_bf16_f32 %0, %1, %2" : "=v"(r) : "v"(lo), "v"(hi)); return r; }
; template <int NET> __device__ __forceinline__ void ret_item(Ctx& F, int item) {
;     ...
;         const int c = 16 * w + fr;
;         bf16x8 pb[4];
; #pragma unroll
;         for (int sk = 0; sk < 4; ++sk) { unsigned pw[4];
; #pragma unroll
;             for (int hlf = 0; hlf < 2; ++hlf) { const int mt = 2 * sk + hlf; float pv[4];
; #pragma unroll
;                 for (int rr = 0; rr < 4; ++rr) { const int m = 16 * mt + 4 * fq + rr; pv[rr] = (c >= m) ? sacc[mt][rr] * dcm[mt][rr] : 0.f; }
;                 pw[2 * hlf] = pk2(pv[0], pv[1]); pw[2 * hlf + 1] = pk2(pv[2], pv[3]); }
;             pb[sk] = __builtin_bit_cast(bf16x8, (u32x4){pw[0], pw[1], pw[2], pw[3]}); }
;         { bf16x8 bqf[4];
; #pragma unroll
;           for (int ks = 0; ks < 4; ++ks) bqf[ks] = *(const LAS bf16x8*)(qL + (16 * w + fr) * LP + 32 * ks + 8 * fq);
;           const float qd = __builtin_amdgcn_exp2f(lg2 * (float)(c + 1));
; #pragma unroll
;           for (int et = 0; et < NET; ++et) { f32x4 oi = (f32x4){0.f, 0.f, 0.f, 0.f}, oc = (f32x4){0.f, 0.f, 0.f, 0.f};
;             bf16x8 avq[4]; const unsigned a0 = vLb + (unsigned)((4 * fq) * (VP * 2) + 32 * et); tr_quad(avq, a0, a0 + 32 * (VP * 2), a0 + 64 * (VP * 2), a0 + 96 * (VP * 2), 16 * (VP * 2));
; #pragma unroll
;             for (int ks = 0; ks < 4; ++ks) { const bf16x8 as = *(const LAS bf16x8*)(STL + (16 * et + fr) * LP + 32 * ks + 8 * fq);
;                 oi = __builtin_amdgcn_mfma_f32_16x16x32_bf16(avq[ks], pb[ks], oi, 0, 0, 0); oc = __builtin_amdgcn_mfma_f32_16x16x32_bf16(as, bqf[ks], oc, 0, 0, 0); }
;             *(f32x4*)(reto + (size_t)(t0 + c) * RW + h * 128 + eb * EW + 16 * et + 4 * fq) = oi + oc * qd; } }
	v_mfma_f32_16x16x32_bf16 v[82:85], v[236:239], v[232:235], v[82:85]
	ds_read_b128 v[236:239], v187 offset:43712
	s_waitcnt lgkmcnt(0)
	v_mfma_f32_16x16x32_bf16 v[86:89], v[236:239], v[232:235], v[86:89]
	ds_read_b128 v[236:239], v187 offset:48064
	s_waitcnt lgkmcnt(0)
	v_mfma_f32_16x16x32_bf16 v[90:93], v[236:239], v[232:235], v[90:93]
	ds_read_b128 v[236:239], v187 offset:52416
	s_waitcnt lgkmcnt(0)
	v_mfma_f32_16x16x32_bf16 v[94:97], v[236:239], v[232:235], v[94:97]
	ds_read_b128 v[236:239], v187 offset:56768
	s_waitcnt lgkmcnt(0)
	v_mfma_f32_16x16x32_bf16 v[98:101], v[236:239], v[232:235], v[98:101]
	ds_read_b128 v[236:239], v187 offset:61120
	s_waitcnt lgkmcnt(0)
	v_mfma_f32_16x16x32_bf16 v[102:105], v[236:239], v[232:235], v[102:105]
	ds_read_b128 v[236:239], v187 offset:65472
	s_waitcnt lgkmcnt(0)
	v_mfma_f32_16x16x32_bf16 v[232:235], v[236:239], v[232:235], v[74:77]
	s_nop 2
	v_mul_f32_e32 v74, v196, v78
	v_mul_f32_e32 v75, v197, v79
	v_mul_f32_e32 v76, v198, v80
	v_mul_f32_e32 v77, v199, v81
	v_cndmask_b32_e64 v74, v74, 0, vcc
	v_cndmask_b32_e64 v75, 0, v75, s[66:67]
	v_cndmask_b32_e64 v76, v76, 0, s[4:5]
	v_cndmask_b32_e64 v77, v77, 0, s[6:7]
	v_cvt_pk_bf16_f32 v74, v74, v75
	v_cvt_pk_bf16_f32 v75, v76, v77
	v_mul_f32_e32 v76, v200, v82
	v_mul_f32_e32 v77, v201, v83
	v_mul_f32_e32 v78, v202, v84
	v_mul_f32_e32 v79, v203, v85
	v_cndmask_b32_e64 v76, v76, 0, s[8:9]
	v_cndmask_b32_e64 v77, v77, 0, s[10:11]
	v_cndmask_b32_e64 v78, v78, 0, s[12:13]
	v_cndmask_b32_e64 v79, v79, 0, s[14:15]
	v_cvt_pk_bf16_f32 v76, v76, v77
	v_cvt_pk_bf16_f32 v77, v78, v79
	v_mul_f32_e32 v78, v204, v86
	v_mul_f32_e32 v79, v205, v87
	v_mul_f32_e32 v80, v206, v88
	v_mul_f32_e32 v81, v207, v89
	v_cndmask_b32_e64 v78, v78, 0, s[16:17]
	v_cndmask_b32_e64 v79, v79, 0, s[18:19]
	v_cndmask_b32_e64 v80, v80, 0, s[20:21]
	v_cndmask_b32_e64 v81, v81, 0, s[22:23]
	v_cvt_pk_bf16_f32 v78, v78, v79
	v_cvt_pk_bf16_f32 v79, v80, v81
	v_mul_f32_e32 v80, v208, v90
	v_mul_f32_e32 v81, v209, v91
	v_mul_f32_e32 v82, v210, v92
	v_mul_f32_e32 v83, v211, v93
	v_cndmask_b32_e64 v80, v80, 0, s[24:25]
	v_cndmask_b32_e64 v81, v81, 0, s[26:27]
	v_cndmask_b32_e64 v82, v82, 0, s[28:29]
	v_cndmask_b32_e64 v83, v83, 0, s[30:31]
	v_cvt_pk_bf16_f32 v80, v80, v81
	v_cvt_pk_bf16_f32 v81, v82, v83
	v_mul_f32_e32 v82, v212, v94
	v_mul_f32_e32 v83, v213, v95
	v_mul_f32_e32 v84, v214, v96
	v_mul_f32_e32 v85, v215, v97
	v_cndmask_b32_e64 v82, v82, 0, s[34:35]
	v_cndmask_b32_e64 v83, v83, 0, s[36:37]
	v_cndmask_b32_e64 v84, v84, 0, s[38:39]
	v_cndmask_b32_e64 v85, v85, 0, s[40:41]
	v_cvt_pk_bf16_f32 v82, v82, v83
	v_cvt_pk_bf16_f32 v83, v84, v85
	v_mul_f32_e32 v84, v216, v98
	v_mul_f32_e32 v85, v217, v99
	v_mul_f32_e32 v86, v218, v100
	v_mul_f32_e32 v87, v219, v101
	v_cndmask_b32_e64 v84, v84, 0, s[42:43]
	v_cndmask_b32_e64 v85, v85, 0, s[44:45]
	v_cndmask_b32_e64 v86, v86, 0, s[46:47]
	v_cndmask_b32_e64 v87, v87, 0, s[48:49]
	v_cvt_pk_bf16_f32 v84, v84, v85
	v_cvt_pk_bf16_f32 v85, v86, v87
	v_mul_f32_e32 v86, v220, v102
	v_mul_f32_e32 v87, v221, v103
	v_mul_f32_e32 v88, v222, v104
	v_mul_f32_e32 v89, v223, v105
	v_cndmask_b32_e64 v86, v86, 0, s[50:51]
	v_cndmask_b32_e64 v87, v87, 0, s[52:53]
	v_cndmask_b32_e64 v88, v88, 0, s[54:55]
	v_cndmask_b32_e64 v89, v89, 0, s[56:57]
	v_cvt_pk_bf16_f32 v86, v86, v87
	v_cvt_pk_bf16_f32 v87, v88, v89
	v_mul_f32_e32 v88, v224, v232
	v_mul_f32_e32 v89, v225, v233
	v_mul_f32_e32 v90, v226, v234
	v_cndmask_b32_e64 v88, v88, 0, s[58:59]
	v_cndmask_b32_e64 v89, v89, 0, s[60:61]
	v_cndmask_b32_e64 v90, v90, 0, s[62:63]
	v_mul_f32_e32 v91, v113, v235
	v_cndmask_b32_e64 v91, v91, 0, s[64:65]
	v_cvt_pk_bf16_f32 v88, v88, v89
	v_cvt_pk_bf16_f32 v89, v90, v91
	v_add_u32_e32 v90, v162, v164
	ds_read_b128 v[102:105], v90
	ds_read_b128 v[98:101], v90 offset:64
	ds_read_b128 v[94:97], v90 offset:128
	ds_read_b128 v[90:93], v90 offset:192
	ds_read_b64_tr_b16 v[244:245], v166
	ds_read_b64_tr_b16 v[246:247], v132
	ds_read_b64_tr_b16 v[240:241], v115
	ds_read_b64_tr_b16 v[242:243], v133
	ds_read_b64_tr_b16 v[236:237], v130
	ds_read_b64_tr_b16 v[238:239], v248
	ds_read_b64_tr_b16 v[232:233], v131
	ds_read_b64_tr_b16 v[234:235], v249
	s_waitcnt lgkmcnt(0)
	ds_read_b128 v[248:251], v188
	ds_read_b128 v[130:133], v188 offset:64
	v_mfma_f32_16x16x32_bf16 v[244:247], v[244:247], v[74:77], 0
	v_add_u32_e32 v115, 32, v166
	v_mfma_f32_16x16x32_bf16 v[240:243], v[240:243], v[78:81], v[244:247]
	s_waitcnt lgkmcnt(1)
	v_mfma_f32_16x16x32_bf16 v[248:251], v[248:251], v[102:105], 0
	s_nop 3
	ds_read_b128 v[244:247], v188 offset:128
	v_mfma_f32_16x16x32_bf16 v[236:239], v[236:239], v[82:85], v[240:243]
	s_nop 2
	ds_read_b128 v[240:243], v188 offset:192
	s_waitcnt lgkmcnt(2)
	v_mfma_f32_16x16x32_bf16 v[130:133], v[130:133], v[98:101], v[248:251]
	s_waitcnt lgkmcnt(1)
	v_mfma_f32_16x16x32_bf16 v[130:133], v[244:247], v[94:97], v[130:133]
	v_add_u32_e32 v244, 0x1220, v166
	v_add_u32_e32 v245, 0x2420, v166
	v_add_u32_e32 v246, 0x3620, v166
	v_mfma_f32_16x16x32_bf16 v[232:235], v[232:235], v[86:89], v[236:239]
	v_add_u32_e32 v247, 0x920, v166
	v_add_u32_e32 v248, 0x1b20, v166
	v_add_u32_e32 v249, 0x2d20, v166
	s_waitcnt lgkmcnt(0)
	v_mfma_f32_16x16x32_bf16 v[130:133], v[240:243], v[90:93], v[130:133]
	v_add_u32_e32 v250, 0x3f20, v166
	s_nop 6
	v_pk_fma_f32 v[132:133], v[118:119], v[132:133], v[234:235]
	v_pk_fma_f32 v[130:131], v[116:117], v[130:131], v[232:233]
	global_store_dwordx4 v[124:125], v[130:133], off
	s_nop 1
	ds_read_b64_tr_b16 v[240:241], v115
	ds_read_b64_tr_b16 v[242:243], v247
	ds_read_b64_tr_b16 v[236:237], v244
	ds_read_b64_tr_b16 v[238:239], v248
	ds_read_b64_tr_b16 v[232:233], v245
	ds_read_b64_tr_b16 v[234:235], v249
	ds_read_b64_tr_b16 v[130:131], v246
	ds_read_b64_tr_b16 v[132:133], v250
	s_waitcnt lgkmcnt(0)
; #define LAS __attribute__((address_space(3)))
; #define LDS_BARRIER() do { asm volatile("s_waitcnt lgkmcnt(0)" ::: "memory"); __builtin_amdgcn_s_barrier(); asm volatile("" ::: "memory"); } while (0)
; template <int NET> __device__ __forceinline__ void ret_item(Ctx& F, int item) {
;     ...
;           for (int et = 0; et < NET; ++et) { f32x4 oi = (f32x4){0.f, 0.f, 0.f, 0.f}, oc = (f32x4){0.f, 0.f, 0.f, 0.f};
;             bf16x8 avq[4]; const unsigned a0 = vLb + (unsigned)((4 * fq) * (VP * 2) + 32 * et); tr_quad(avq, a0, a0 + 32 * (VP * 2), a0 + 64 * (VP * 2), a0 + 96 * (VP * 2), 16 * (VP * 2));
; #pragma unroll
;             for (int ks = 0; ks < 4; ++ks) { const bf16x8 as = *(const LAS bf16x8*)(STL + (16 * et + fr) * LP + 32 * ks + 8 * fq);
;                 oi = __builtin_amdgcn_mfma_f32_16x16x32_bf16(avq[ks], pb[ks], oi, 0, 0, 0); oc = __builtin_amdgcn_mfma_f32_16x16x32_bf16(as, bqf[ks], oc, 0, 0, 0); }
;             *(f32x4*)(reto + (size_t)(t0 + c) * RW + h * 128 + eb * EW + 16 * et + 4 * fq) = oi + oc * qd; } }
;         LDS_BARRIER();
; #pragma unroll
;         for (int et = 0; et < NET; ++et) st[et] = st[et] * dec;
	ds_read_b128 v[244:247], v188 offset:4352
	ds_read_b128 v[248:251], v188 offset:4416
	v_mfma_f32_16x16x32_bf16 v[240:243], v[240:243], v[74:77], 0
	v_add_u32_e32 v115, 64, v166
	s_waitcnt lgkmcnt(1)
	v_mfma_f32_16x16x32_bf16 v[244:247], v[244:247], v[102:105], 0
	v_mfma_f32_16x16x32_bf16 v[236:239], v[236:239], v[78:81], v[240:243]
	s_waitcnt lgkmcnt(0)
	v_mfma_f32_16x16x32_bf16 v[240:243], v[248:251], v[98:101], v[244:247]
	v_add_u32_e32 v248, 0x1b40, v166
	v_add_u32_e32 v249, 0x2d40, v166
	v_add_u32_e32 v250, 0x3f40, v166
	s_nop 1
	ds_read_b128 v[244:247], v188 offset:4480
	v_mfma_f32_16x16x32_bf16 v[232:235], v[232:235], v[82:85], v[236:239]
	s_waitcnt lgkmcnt(0)
	v_mfma_f32_16x16x32_bf16 v[236:239], v[244:247], v[94:97], v[240:243]
	s_nop 2
	ds_read_b128 v[240:243], v188 offset:4544
	v_add_u32_e32 v244, 0x1240, v166
	v_add_u32_e32 v245, 0x2440, v166
	v_mfma_f32_16x16x32_bf16 v[130:133], v[130:133], v[86:89], v[232:235]
	v_add_u32_e32 v246, 0x3640, v166
	v_add_u32_e32 v247, 0x940, v166
	s_waitcnt lgkmcnt(0)
	v_mfma_f32_16x16x32_bf16 v[232:235], v[240:243], v[90:93], v[236:239]
	s_nop 7
	v_pk_fma_f32 v[132:133], v[118:119], v[234:235], v[132:133]
	v_pk_fma_f32 v[130:131], v[116:117], v[232:233], v[130:131]
	global_store_dwordx4 v[124:125], v[130:133], off offset:64
	s_nop 1
	ds_read_b64_tr_b16 v[240:241], v115
	ds_read_b64_tr_b16 v[242:243], v247
	ds_read_b64_tr_b16 v[236:237], v244
	ds_read_b64_tr_b16 v[238:239], v248
	ds_read_b64_tr_b16 v[232:233], v245
	ds_read_b64_tr_b16 v[234:235], v249
	ds_read_b64_tr_b16 v[130:131], v246
	ds_read_b64_tr_b16 v[132:133], v250
	s_waitcnt lgkmcnt(0)
	ds_read_b128 v[244:247], v188 offset:8704
	ds_read_b128 v[248:251], v188 offset:8768
	v_mfma_f32_16x16x32_bf16 v[240:243], v[240:243], v[74:77], 0
	v_add_u32_e32 v115, 0x60, v166
	s_waitcnt lgkmcnt(1)
	v_mfma_f32_16x16x32_bf16 v[244:247], v[244:247], v[102:105], 0
	v_mfma_f32_16x16x32_bf16 v[236:239], v[236:239], v[78:81], v[240:243]
	s_waitcnt lgkmcnt(0)
	v_mfma_f32_16x16x32_bf16 v[240:243], v[248:251], v[98:101], v[244:247]
	v_add_u32_e32 v248, 0x1b60, v166
	v_add_u32_e32 v249, 0x2d60, v166
	v_add_u32_e32 v250, 0x3f60, v166
	s_nop 1
	ds_read_b128 v[244:247], v188 offset:8832
	v_mfma_f32_16x16x32_bf16 v[232:235], v[232:235], v[82:85], v[236:239]
	s_waitcnt lgkmcnt(0)
	v_mfma_f32_16x16x32_bf16 v[236:239], v[244:247], v[94:97], v[240:243]
	s_nop 2
	ds_read_b128 v[240:243], v188 offset:8896
	v_add_u32_e32 v244, 0x1260, v166
	v_add_u32_e32 v245, 0x2460, v166
	v_mfma_f32_16x16x32_bf16 v[130:133], v[130:133], v[86:89], v[232:235]
	v_add_u32_e32 v246, 0x3660, v166
	v_add_u32_e32 v247, 0x960, v166
	s_waitcnt lgkmcnt(0)
	v_mfma_f32_16x16x32_bf16 v[232:235], v[240:243], v[90:93], v[236:239]
	s_nop 7
	v_pk_fma_f32 v[132:133], v[118:119], v[234:235], v[132:133]
	v_pk_fma_f32 v[130:131], v[116:117], v[232:233], v[130:131]
	global_store_dwordx4 v[124:125], v[130:133], off offset:128
	s_nop 1
	ds_read_b64_tr_b16 v[240:241], v115
	ds_read_b64_tr_b16 v[242:243], v247
	ds_read_b64_tr_b16 v[236:237], v244
	ds_read_b64_tr_b16 v[238:239], v248
	ds_read_b64_tr_b16 v[232:233], v245
	ds_read_b64_tr_b16 v[234:235], v249
	ds_read_b64_tr_b16 v[130:131], v246
	ds_read_b64_tr_b16 v[132:133], v250
	s_waitcnt lgkmcnt(0)
	ds_read_b128 v[244:247], v188 offset:13056
	v_mfma_f32_16x16x32_bf16 v[74:77], v[240:243], v[74:77], 0
	ds_read_b128 v[240:243], v188 offset:13120
	v_mov_b32_e32 v115, v114
	v_pk_mul_f32 v[12:13], v[114:115], v[12:13]
	s_waitcnt lgkmcnt(1)
	v_mfma_f32_16x16x32_bf16 v[102:105], v[244:247], v[102:105], 0
	v_mul_f32_e64 v16, v114, v16
	v_mul_f32_e64 v17, v115, v17
	v_pk_mul_f32 v[8:9], v[114:115], v[8:9]
	v_pk_mul_f32 v[4:5], v[114:115], v[4:5]
	v_mfma_f32_16x16x32_bf16 v[74:77], v[236:239], v[78:81], v[74:77]
	v_add_u32_e32 v115, 0x1200, v168
	s_waitcnt lgkmcnt(0)
	v_mfma_f32_16x16x32_bf16 v[78:81], v[240:243], v[98:101], v[102:105]
	ds_read_b128 v[98:101], v188 offset:13184
	v_mfma_f32_16x16x32_bf16 v[74:77], v[232:235], v[82:85], v[74:77]
	ds_read_b128 v[82:85], v188 offset:13248
	v_add_u32_e32 v232, 0x3860, v168
	s_waitcnt lgkmcnt(1)
	v_mfma_f32_16x16x32_bf16 v[78:81], v[98:101], v[94:97], v[78:81]
	v_add_u32_e32 v94, 0x2640, v167
	v_add_u32_e32 v95, 0x4840, v167
	v_add_u32_e32 v96, 0x6a40, v167
	v_mfma_f32_16x16x32_bf16 v[74:77], v[130:133], v[86:89], v[74:77]
	v_add_u32_e32 v130, 0x240, v168
	v_add_u32_e32 v131, 0x1440, v168
	v_add_u32_e32 v132, 0x2640, v168
	s_waitcnt lgkmcnt(0)
	v_mfma_f32_16x16x32_bf16 v[78:81], v[82:85], v[90:93], v[78:81]
	v_add_u32_e32 v90, 0x2200, v167
	v_add_u32_e32 v91, 0x4400, v167
	v_add_u32_e32 v92, 0x6600, v167
	v_add_u32_e32 v93, 0x440, v167
	v_add_u32_e32 v133, 0x3840, v168
	s_nop 2
	v_pk_fma_f32 v[76:77], v[118:119], v[80:81], v[76:77]
	v_pk_fma_f32 v[74:75], v[116:117], v[78:79], v[74:75]
	global_store_dwordx4 v[124:125], v[74:77], off offset:192
	s_waitcnt lgkmcnt(0)
	s_barrier
; #define LDS_BARRIER() do { asm volatile("s_waitcnt lgkmcnt(0)" ::: "memory"); __builtin_amdgcn_s_barrier(); asm volatile("" ::: "memory"); } while (0)
; template <int NET> __device__ __forceinline__ void ret_item(Ctx& F, int item) {
;     ...
;         for (int et = 0; et < NET; ++et) st[et] = st[et] * dec;
;         { bf16x8 bkq[4];
;           { const unsigned k0 = kLb + (unsigned)((8 * fq) * (LP * 2)); tr_quad(bkq, k0, k0 + 32 * (LP * 2), k0 + 64 * (LP * 2), k0 + 96 * (LP * 2), 4 * (LP * 2)); }
; #pragma unroll
;           for (int et = 0; et < NET; ++et) { bf16x8 vq[4]; const unsigned v0 = vdLb + (unsigned)((8 * fq) * (VP * 2) + 32 * et); tr_quad(vq, v0, v0 + 32 * (VP * 2), v0 + 64 * (VP * 2), v0 + 96 * (VP * 2), 4 * (VP * 2));
; #pragma unroll
;             for (int ks = 0; ks < 4; ++ks) st[et] = __builtin_amdgcn_mfma_f32_16x16x32_bf16(vq[ks], bkq[ks], st[et], 0, 0, 0); } }
; #pragma unroll
;         for (int et = 0; et < NET; ++et)
; #pragma unroll
;             for (int rr = 0; rr < 4; ++rr) STL[(16 * et + 4 * fq + rr) * LP + 16 * w + fr] = f2bf(st[et][rr]);
;         LDS_BARRIER();
	v_add_u32_e32 v124, 0x2400, v168
	ds_read_b64_tr_b16 v[86:87], v167
	ds_read_b64_tr_b16 v[88:89], v93
	ds_read_b64_tr_b16 v[82:83], v90
	ds_read_b64_tr_b16 v[84:85], v94
	ds_read_b64_tr_b16 v[78:79], v91
	ds_read_b64_tr_b16 v[80:81], v95
	ds_read_b64_tr_b16 v[74:75], v92
	ds_read_b64_tr_b16 v[76:77], v96
	s_waitcnt lgkmcnt(0)
	v_add_u32_e32 v125, 0x3600, v168
	ds_read_b64_tr_b16 v[102:103], v168
	ds_read_b64_tr_b16 v[104:105], v130
	ds_read_b64_tr_b16 v[98:99], v115
	ds_read_b64_tr_b16 v[100:101], v131
	ds_read_b64_tr_b16 v[94:95], v124
	ds_read_b64_tr_b16 v[96:97], v132
	ds_read_b64_tr_b16 v[90:91], v125
	ds_read_b64_tr_b16 v[92:93], v133
	s_waitcnt lgkmcnt(0)
	v_add_u32_e32 v115, 32, v168
	v_mfma_f32_16x16x32_bf16 v[10:13], v[102:105], v[86:89], v[10:13]
	v_add_u32_e32 v124, 0x1220, v168
	v_add_u32_e32 v125, 0x2420, v168
	v_add_u32_e32 v130, 0x3620, v168
	v_mfma_f32_16x16x32_bf16 v[10:13], v[98:101], v[82:85], v[10:13]
	v_add_u32_e32 v131, 0x260, v168
	v_add_u32_e32 v132, 0x1460, v168
	v_add_u32_e32 v133, 0x2660, v168
	v_mfma_f32_16x16x32_bf16 v[10:13], v[94:97], v[78:81], v[10:13]
	v_mfma_f32_16x16x32_bf16 v[10:13], v[90:93], v[74:77], v[10:13]
	ds_read_b64_tr_b16 v[102:103], v115
	ds_read_b64_tr_b16 v[104:105], v131
	ds_read_b64_tr_b16 v[98:99], v124
	ds_read_b64_tr_b16 v[100:101], v132
	ds_read_b64_tr_b16 v[94:95], v125
	ds_read_b64_tr_b16 v[96:97], v133
	ds_read_b64_tr_b16 v[90:91], v130
	ds_read_b64_tr_b16 v[92:93], v232
	s_waitcnt lgkmcnt(0)
	v_add_u32_e32 v115, 64, v168
	v_mfma_f32_16x16x32_bf16 v[14:17], v[102:105], v[86:89], v[14:17]
	v_mfma_f32_16x16x32_bf16 v[14:17], v[98:101], v[82:85], v[14:17]
	v_mfma_f32_16x16x32_bf16 v[14:17], v[94:97], v[78:81], v[14:17]
	v_mfma_f32_16x16x32_bf16 v[14:17], v[90:93], v[74:77], v[14:17]
	ds_read_b64_tr_b16 v[102:103], v115
	ds_read_b64_tr_b16 v[104:105], v172
	ds_read_b64_tr_b16 v[98:99], v169
	ds_read_b64_tr_b16 v[100:101], v173
	ds_read_b64_tr_b16 v[94:95], v170
	ds_read_b64_tr_b16 v[96:97], v174
	ds_read_b64_tr_b16 v[90:91], v171
	ds_read_b64_tr_b16 v[92:93], v175
	s_waitcnt lgkmcnt(0)
	s_nop 0
	v_mfma_f32_16x16x32_bf16 v[6:9], v[102:105], v[86:89], v[6:9]
	v_mfma_f32_16x16x32_bf16 v[6:9], v[98:101], v[82:85], v[6:9]
	v_mfma_f32_16x16x32_bf16 v[6:9], v[94:97], v[78:81], v[6:9]
	v_mfma_f32_16x16x32_bf16 v[6:9], v[90:93], v[74:77], v[6:9]
	ds_read_b64_tr_b16 v[102:103], v176
	ds_read_b64_tr_b16 v[104:105], v180
	ds_read_b64_tr_b16 v[98:99], v177
	ds_read_b64_tr_b16 v[100:101], v181
	ds_read_b64_tr_b16 v[94:95], v178
	ds_read_b64_tr_b16 v[96:97], v182
	ds_read_b64_tr_b16 v[90:91], v179
	ds_read_b64_tr_b16 v[92:93], v183
	s_waitcnt lgkmcnt(0)
	s_nop 0
	v_mfma_f32_16x16x32_bf16 v[2:5], v[102:105], v[86:89], v[2:5]
	v_mfma_f32_16x16x32_bf16 v[2:5], v[98:101], v[82:85], v[2:5]
	v_mfma_f32_16x16x32_bf16 v[2:5], v[94:97], v[78:81], v[2:5]
	s_waitcnt vmcnt(14)
	v_lshlrev_b32_e32 v79, 16, v54
	v_lshlrev_b32_e32 v78, 16, v50
	v_mfma_f32_16x16x32_bf16 v[2:5], v[90:93], v[74:77], v[2:5]
	v_cvt_pk_bf16_f32 v74, v10, s0
	ds_write_b16 v189, v74
	v_cvt_pk_bf16_f32 v74, v11, s0
	ds_write_b16 v190, v74
	v_cvt_pk_bf16_f32 v74, v12, s0
	ds_write_b16 v190, v74 offset:272
	v_cvt_pk_bf16_f32 v74, v13, s0
	ds_write_b16 v190, v74 offset:544
	v_cvt_pk_bf16_f32 v74, v14, s0
	ds_write_b16 v190, v74 offset:4080
	v_cvt_pk_bf16_f32 v74, v15, s0
	ds_write_b16 v190, v74 offset:4352
	v_cvt_pk_bf16_f32 v74, v16, s0
	ds_write_b16 v190, v74 offset:4624
	v_cvt_pk_bf16_f32 v74, v17, s0
	ds_write_b16 v190, v74 offset:4896
	v_cvt_pk_bf16_f32 v74, v6, s0
	ds_write_b16 v190, v74 offset:8432
	v_cvt_pk_bf16_f32 v74, v7, s0
	ds_write_b16 v190, v74 offset:8704
	v_cvt_pk_bf16_f32 v74, v8, s0
	ds_write_b16 v190, v74 offset:8976
	v_cvt_pk_bf16_f32 v74, v9, s0
	ds_write_b16 v190, v74 offset:9248
	v_cvt_pk_bf16_f32 v74, v2, s0
	ds_write_b16 v190, v74 offset:12784
	v_cvt_pk_bf16_f32 v74, v3, s0
	ds_write_b16 v190, v74 offset:13056
	v_cvt_pk_bf16_f32 v74, v4, s0
	ds_write_b16 v190, v74 offset:13328
	v_cvt_pk_bf16_f32 v74, v5, s0
	ds_write_b16 v190, v74 offset:13600
	s_waitcnt vmcnt(4)
	v_and_b32_e32 v74, 0xffff0000, v70
	v_lshlrev_b32_e32 v75, 16, v70
	v_pk_mul_f32 v[80:81], v[74:75], v[78:79] op_sel:[1,0] op_sel_hi:[0,1]
	v_sub_f32_e32 v70, v80, v81
	v_pk_mul_f32 v[78:79], v[78:79], v[74:75]
	v_lshlrev_b32_e32 v77, 16, v62
	v_lshlrev_b32_e32 v76, 16, v58
	v_mul_f32_e32 v80, 0x3db504f3, v70
	v_add_f32_e32 v70, v78, v79
	v_mul_f32_e32 v81, 0x3db504f3, v70
	v_pk_mul_f32 v[78:79], v[74:75], v[76:77] op_sel:[1,0] op_sel_hi:[0,1]
	v_pk_mul_f32 v[74:75], v[76:77], v[74:75]
	v_and_b32_e32 v70, 0xffff0000, v71
	v_lshlrev_b32_e32 v71, 16, v71
	v_and_b32_e32 v77, 0xffff0000, v54
	v_and_b32_e32 v76, 0xffff0000, v50
	v_sub_f32_e32 v82, v78, v79
	v_add_f32_e32 v83, v74, v75
	v_and_b32_e32 v75, 0xffff0000, v62
	v_and_b32_e32 v74, 0xffff0000, v58
	v_pk_mul_f32 v[78:79], v[70:71], v[76:77] op_sel:[1,0] op_sel_hi:[0,1]
	v_pk_mul_f32 v[76:77], v[76:77], v[70:71]
	v_sub_f32_e32 v50, v78, v79
	v_add_f32_e32 v54, v76, v77
	v_pk_mul_f32 v[76:77], v[70:71], v[74:75] op_sel:[1,0] op_sel_hi:[0,1]
	v_pk_mul_f32 v[70:71], v[74:75], v[70:71]
	v_mul_f32_e32 v50, 0x3db504f3, v50
	v_mul_f32_e32 v54, 0x3db504f3, v54
	v_sub_f32_e32 v76, v76, v77
	v_add_f32_e32 v70, v70, v71
	s_waitcnt lgkmcnt(0)
	s_barrier
; #define LAS __attribute__((address_space(3)))
; __device__ __forceinline__ unsigned pk2(float lo, float hi) { unsigned r; asm volatile("v_cvt_pk_bf16_f32 %0, %1, %2" : "=v"(r) : "v"(lo), "v"(hi)); return r; }
; __device__ __forceinline__ float bflo(unsigned w) { return __uint_as_float(w << 16); }
; __device__ __forceinline__ float bfhi(unsigned w) { return __uint_as_float(w & 0xffff0000u); }
; template <int NET> __device__ __forceinline__ void ret_item(Ctx& F, int item) {
;     ...
;             for (int hh = 0; hh < 2; ++hh) { unsigned oq1[4], oq2[4], ok1[4], ok2[4];
; #pragma unroll
;                 for (int c = 0; c < 4; ++c) { float a[2], bq[2], ka[2], kb[2];
; #pragma unroll
;                     for (int z = 0; z < 2; ++z) { const int jj = hh * 8 + c * 2 + z; const unsigned cw_ = cs4[jj >> 2][jj & 3]; const f32x2 sc = (f32x2){bflo(cw_), bfhi(cw_)};
;                         const float x1 = z ? bfhi(q1[hh][c]) : bflo(q1[hh][c]), x2 = z ? bfhi(q2[hh][c]) : bflo(q2[hh][c]);
;                         const float y1 = z ? bfhi(k1[hh][c]) : bflo(k1[hh][c]), y2 = z ? bfhi(k2[hh][c]) : bflo(k2[hh][c]);
;                         a[z] = (x1 * sc.x - x2 * sc.y) * 0.08838834764831845f; bq[z] = (x2 * sc.x + x1 * sc.y) * 0.08838834764831845f;
;                         ka[z] = y1 * sc.x - y2 * sc.y; kb[z] = y2 * sc.x + y1 * sc.y;
;                     }
;                     oq1[c] = pk2(a[0], a[1]); oq2[c] = pk2(bq[0], bq[1]); ok1[c] = pk2(ka[0], ka[1]); ok2[c] = pk2(kb[0], kb[1]); }
;     ...
;             for (int vi = 0; vi < NET / 2; ++vi) { unsigned vd[4];
; #pragma unroll
;                 for (int c = 0; c < 4; ++c) vd[c] = pk2(bflo(vv[vi][c]) * kdec, bfhi(vv[vi][c]) * kdec);
;                 *(LAS u32x4*)(vL + r * VP + qd * (EW / 4) + 8 * vi) = vv[vi]; *(LAS u32x4*)(vdL + r * VP + qd * (EW / 4) + 8 * vi) = (u32x4){vd[0], vd[1], vd[2], vd[3]}; }
	v_lshlrev_b32_e32 v92, 16, v22
	v_and_b32_e32 v93, 0xffff0000, v22
	v_mul_f32_e32 v92, v227, v92
	v_mul_f32_e32 v93, v227, v93
	v_cvt_pk_bf16_f32 v84, v92, v93
	v_lshlrev_b32_e32 v92, 16, v23
	v_and_b32_e32 v93, 0xffff0000, v23
	v_mul_f32_e32 v92, v227, v92
	v_mul_f32_e32 v93, v227, v93
	v_cvt_pk_bf16_f32 v85, v92, v93
	v_lshlrev_b32_e32 v92, 16, v24
	v_and_b32_e32 v93, 0xffff0000, v24
	v_mul_f32_e32 v92, v227, v92
	v_mul_f32_e32 v93, v227, v93
	v_cvt_pk_bf16_f32 v86, v92, v93
	v_lshlrev_b32_e32 v92, 16, v25
	v_and_b32_e32 v93, 0xffff0000, v25
	v_mul_f32_e32 v92, v227, v92
	v_mul_f32_e32 v93, v227, v93
	v_cvt_pk_bf16_f32 v87, v92, v93
	ds_write_b128 v194, v[22:25]
	ds_write_b128 v195, v[84:87]
	v_lshlrev_b32_e32 v92, 16, v18
	v_and_b32_e32 v93, 0xffff0000, v18
	v_mul_f32_e32 v92, v227, v92
	v_mul_f32_e32 v93, v227, v93
	v_cvt_pk_bf16_f32 v88, v92, v93
	v_lshlrev_b32_e32 v92, 16, v19
	v_and_b32_e32 v93, 0xffff0000, v19
	v_mul_f32_e32 v92, v227, v92
	v_mul_f32_e32 v93, v227, v93
	v_cvt_pk_bf16_f32 v89, v92, v93
	v_lshlrev_b32_e32 v92, 16, v20
	v_and_b32_e32 v93, 0xffff0000, v20
	v_mul_f32_e32 v92, v227, v92
	v_mul_f32_e32 v93, v227, v93
	v_cvt_pk_bf16_f32 v90, v92, v93
	v_lshlrev_b32_e32 v92, 16, v21
	v_and_b32_e32 v93, 0xffff0000, v21
	v_mul_f32_e32 v92, v227, v92
	v_mul_f32_e32 v93, v227, v93
	v_cvt_pk_bf16_f32 v91, v92, v93
	ds_write_b128 v194, v[18:21] offset:16
	ds_write_b128 v195, v[88:91] offset:16
	v_cvt_pk_bf16_f32 v62, v80, v50
	v_cvt_pk_bf16_f32 v58, v81, v54
	v_cvt_pk_bf16_f32 v54, v82, v76
	v_cvt_pk_bf16_f32 v50, v83, v70
	v_and_b32_e32 v70, 0xffff0000, v72
	v_lshlrev_b32_e32 v71, 16, v72
	v_lshlrev_b32_e32 v77, 16, v55
	v_lshlrev_b32_e32 v76, 16, v51
	v_pk_mul_f32 v[78:79], v[70:71], v[76:77] op_sel:[1,0] op_sel_hi:[0,1]
	v_lshlrev_b32_e32 v75, 16, v63
	v_lshlrev_b32_e32 v74, 16, v59
	v_sub_f32_e32 v72, v78, v79
	v_pk_mul_f32 v[76:77], v[76:77], v[70:71]
	v_mul_f32_e32 v78, 0x3db504f3, v72
	v_add_f32_e32 v72, v76, v77
	v_pk_mul_f32 v[76:77], v[70:71], v[74:75] op_sel:[1,0] op_sel_hi:[0,1]
	v_pk_mul_f32 v[70:71], v[74:75], v[70:71]
	v_and_b32_e32 v75, 0xffff0000, v55
	v_add_f32_e32 v81, v70, v71
	v_and_b32_e32 v70, 0xffff0000, v73
	v_lshlrev_b32_e32 v71, 16, v73
	v_and_b32_e32 v74, 0xffff0000, v51
	v_mul_f32_e32 v79, 0x3db504f3, v72
	v_sub_f32_e32 v80, v76, v77
	v_and_b32_e32 v73, 0xffff0000, v63
	v_and_b32_e32 v72, 0xffff0000, v59
	v_pk_mul_f32 v[76:77], v[70:71], v[74:75] op_sel:[1,0] op_sel_hi:[0,1]
	v_pk_mul_f32 v[74:75], v[74:75], v[70:71]
	v_sub_f32_e32 v51, v76, v77
	v_add_f32_e32 v55, v74, v75
	v_pk_mul_f32 v[74:75], v[70:71], v[72:73] op_sel:[1,0] op_sel_hi:[0,1]
	v_pk_mul_f32 v[70:71], v[72:73], v[70:71]
	v_mul_f32_e32 v51, 0x3db504f3, v51
	v_mul_f32_e32 v55, 0x3db504f3, v55
	v_sub_f32_e32 v74, v74, v75
	v_add_f32_e32 v70, v70, v71
	v_cvt_pk_bf16_f32 v63, v78, v51
	v_cvt_pk_bf16_f32 v59, v79, v55
	v_cvt_pk_bf16_f32 v55, v80, v74
	v_cvt_pk_bf16_f32 v51, v81, v70
	v_and_b32_e32 v70, 0xffff0000, v66
	v_lshlrev_b32_e32 v71, 16, v66
	v_lshlrev_b32_e32 v75, 16, v56
	v_lshlrev_b32_e32 v74, 16, v52
	v_pk_mul_f32 v[76:77], v[70:71], v[74:75] op_sel:[1,0] op_sel_hi:[0,1]
	v_sub_f32_e32 v66, v76, v77
	v_pk_mul_f32 v[74:75], v[74:75], v[70:71]
	v_lshlrev_b32_e32 v73, 16, v64
	v_lshlrev_b32_e32 v72, 16, v60
	v_mul_f32_e32 v76, 0x3db504f3, v66
	v_add_f32_e32 v66, v74, v75
	v_mul_f32_e32 v77, 0x3db504f3, v66
	v_pk_mul_f32 v[74:75], v[70:71], v[72:73] op_sel:[1,0] op_sel_hi:[0,1]
	v_pk_mul_f32 v[70:71], v[72:73], v[70:71]
	v_and_b32_e32 v66, 0xffff0000, v67
	v_lshlrev_b32_e32 v67, 16, v67
	v_and_b32_e32 v73, 0xffff0000, v56
	v_and_b32_e32 v72, 0xffff0000, v52
	v_sub_f32_e32 v78, v74, v75
	v_add_f32_e32 v79, v70, v71
	v_and_b32_e32 v71, 0xffff0000, v64
	v_and_b32_e32 v70, 0xffff0000, v60
	v_pk_mul_f32 v[74:75], v[66:67], v[72:73] op_sel:[1,0] op_sel_hi:[0,1]
	v_pk_mul_f32 v[72:73], v[72:73], v[66:67]
	v_sub_f32_e32 v52, v74, v75
	v_add_f32_e32 v56, v72, v73
	v_pk_mul_f32 v[72:73], v[66:67], v[70:71] op_sel:[1,0] op_sel_hi:[0,1]
	v_pk_mul_f32 v[66:67], v[70:71], v[66:67]
	v_mul_f32_e32 v52, 0x3db504f3, v52
	v_mul_f32_e32 v56, 0x3db504f3, v56
	v_sub_f32_e32 v72, v72, v73
	v_add_f32_e32 v66, v66, v67
	v_cvt_pk_bf16_f32 v64, v76, v52
	v_cvt_pk_bf16_f32 v60, v77, v56
	v_cvt_pk_bf16_f32 v56, v78, v72
	v_cvt_pk_bf16_f32 v52, v79, v66
	v_and_b32_e32 v66, 0xffff0000, v68
	v_lshlrev_b32_e32 v67, 16, v68
	v_lshlrev_b32_e32 v73, 16, v57
	v_lshlrev_b32_e32 v72, 16, v53
	v_pk_mul_f32 v[74:75], v[66:67], v[72:73] op_sel:[1,0] op_sel_hi:[0,1]
	v_lshlrev_b32_e32 v71, 16, v65
	v_lshlrev_b32_e32 v70, 16, v61
	v_sub_f32_e32 v68, v74, v75
	v_pk_mul_f32 v[72:73], v[72:73], v[66:67]
	v_mul_f32_e32 v74, 0x3db504f3, v68
	v_add_f32_e32 v68, v72, v73
	v_pk_mul_f32 v[72:73], v[66:67], v[70:71] op_sel:[1,0] op_sel_hi:[0,1]
	v_pk_mul_f32 v[66:67], v[70:71], v[66:67]
	v_and_b32_e32 v71, 0xffff0000, v57
	v_add_f32_e32 v77, v66, v67
	v_and_b32_e32 v66, 0xffff0000, v69
	v_lshlrev_b32_e32 v67, 16, v69
	v_and_b32_e32 v70, 0xffff0000, v53
	v_sub_f32_e32 v76, v72, v73
	v_pk_mul_f32 v[72:73], v[66:67], v[70:71] op_sel:[1,0] op_sel_hi:[0,1]
	v_pk_mul_f32 v[70:71], v[70:71], v[66:67]
	v_mul_f32_e32 v75, 0x3db504f3, v68
	v_and_b32_e32 v69, 0xffff0000, v65
	v_and_b32_e32 v68, 0xffff0000, v61
	v_sub_f32_e32 v53, v72, v73
	v_add_f32_e32 v57, v70, v71
	v_mul_f32_e32 v53, 0x3db504f3, v53
	v_mul_f32_e32 v57, 0x3db504f3, v57
	v_pk_mul_f32 v[70:71], v[66:67], v[68:69] op_sel:[1,0] op_sel_hi:[0,1]
	v_pk_mul_f32 v[66:67], v[68:69], v[66:67]
	v_sub_f32_e32 v70, v70, v71
	v_add_f32_e32 v66, v66, v67
	v_cvt_pk_bf16_f32 v65, v74, v53
	v_cvt_pk_bf16_f32 v61, v75, v57
	v_cvt_pk_bf16_f32 v57, v76, v70
; #define LAS __attribute__((address_space(3)))
; __device__ __forceinline__ unsigned pk2(float lo, float hi) { unsigned r; asm volatile("v_cvt_pk_bf16_f32 %0, %1, %2" : "=v"(r) : "v"(lo), "v"(hi)); return r; }
; __device__ __forceinline__ float bflo(unsigned w) { return __uint_as_float(w << 16); }
; __device__ __forceinline__ float bfhi(unsigned w) { return __uint_as_float(w & 0xffff0000u); }
; template <int NET> __device__ __forceinline__ void ret_item(Ctx& F, int item) {
;     ...
;             for (int hh = 0; hh < 2; ++hh) { unsigned oq1[4], oq2[4], ok1[4], ok2[4];
; #pragma unroll
;                 for (int c = 0; c < 4; ++c) { float a[2], bq[2], ka[2], kb[2];
; #pragma unroll
;                     for (int z = 0; z < 2; ++z) { const int jj = hh * 8 + c * 2 + z; const unsigned cw_ = cs4[jj >> 2][jj & 3]; const f32x2 sc = (f32x2){bflo(cw_), bfhi(cw_)};
;                         const float x1 = z ? bfhi(q1[hh][c]) : bflo(q1[hh][c]), x2 = z ? bfhi(q2[hh][c]) : bflo(q2[hh][c]);
;                         const float y1 = z ? bfhi(k1[hh][c]) : bflo(k1[hh][c]), y2 = z ? bfhi(k2[hh][c]) : bflo(k2[hh][c]);
;                         a[z] = (x1 * sc.x - x2 * sc.y) * 0.08838834764831845f; bq[z] = (x2 * sc.x + x1 * sc.y) * 0.08838834764831845f;
;                         ka[z] = y1 * sc.x - y2 * sc.y; kb[z] = y2 * sc.x + y1 * sc.y;
;                     }
;                     oq1[c] = pk2(a[0], a[1]); oq2[c] = pk2(bq[0], bq[1]); ok1[c] = pk2(ka[0], ka[1]); ok2[c] = pk2(kb[0], kb[1]); }
;                 *(LAS u32x4*)(qL + r * LP + j0 + hh * 8) = (u32x4){oq1[0], oq1[1], oq1[2], oq1[3]}; *(LAS u32x4*)(qL + r * LP + 64 + j0 + hh * 8) = (u32x4){oq2[0], oq2[1], oq2[2], oq2[3]};
;                 *(LAS u32x4*)(kL + r * LP + j0 + hh * 8) = (u32x4){ok1[0], ok1[1], ok1[2], ok1[3]}; *(LAS u32x4*)(kL + r * LP + 64 + j0 + hh * 8) = (u32x4){ok2[0], ok2[1], ok2[2], ok2[3]}; }
;     ...
;         ret_stage();
;     }
;     ...
;     __syncthreads();
; }
	v_cvt_pk_bf16_f32 v53, v77, v66
	ds_write_b128 v161, v[62:65]
	ds_write_b128 v161, v[58:61] offset:128
	ds_write_b128 v161, v[54:57] offset:34816
	ds_write_b128 v161, v[50:53] offset:34944
	v_lshlrev_b32_e32 v50, 16, v46
	v_and_b32_e32 v51, 0xffff0000, v46
	v_lshlrev_b32_e32 v53, 16, v30
	v_lshlrev_b32_e32 v52, 16, v26
	v_pk_mul_f32 v[54:55], v[52:53], v[50:51]
	v_pk_mul_f32 v[52:53], v[50:51], v[52:53] op_sel:[1,0] op_sel_hi:[0,1]
	v_sub_f32_e32 v46, v54, v55
	v_mul_f32_e32 v56, 0x3db504f3, v46
	v_add_f32_e32 v46, v52, v53
	v_lshlrev_b32_e32 v53, 16, v38
	v_lshlrev_b32_e32 v52, 16, v34
	v_pk_mul_f32 v[54:55], v[52:53], v[50:51]
	v_pk_mul_f32 v[50:51], v[50:51], v[52:53] op_sel:[1,0] op_sel_hi:[0,1]
	v_mul_f32_e32 v57, 0x3db504f3, v46
	v_sub_f32_e32 v54, v54, v55
	v_add_f32_e32 v55, v50, v51
	v_lshlrev_b32_e32 v46, 16, v47
	v_and_b32_e32 v47, 0xffff0000, v47
	v_and_b32_e32 v51, 0xffff0000, v30
	v_and_b32_e32 v50, 0xffff0000, v26
	v_pk_mul_f32 v[52:53], v[50:51], v[46:47]
	v_pk_mul_f32 v[50:51], v[46:47], v[50:51] op_sel:[1,0] op_sel_hi:[0,1]
	v_add_f32_e32 v30, v50, v51
	v_and_b32_e32 v51, 0xffff0000, v38
	v_and_b32_e32 v50, 0xffff0000, v34
	v_sub_f32_e32 v26, v52, v53
	v_pk_mul_f32 v[52:53], v[50:51], v[46:47]
	v_pk_mul_f32 v[46:47], v[46:47], v[50:51] op_sel:[1,0] op_sel_hi:[0,1]
	v_mul_f32_e32 v26, 0x3db504f3, v26
	v_mul_f32_e32 v30, 0x3db504f3, v30
	v_add_f32_e32 v46, v46, v47
	v_sub_f32_e32 v52, v52, v53
	v_cvt_pk_bf16_f32 v38, v56, v26
	v_cvt_pk_bf16_f32 v34, v57, v30
	v_cvt_pk_bf16_f32 v30, v54, v52
	v_cvt_pk_bf16_f32 v26, v55, v46
	v_lshlrev_b32_e32 v46, 16, v48
	v_and_b32_e32 v47, 0xffff0000, v48
	v_lshlrev_b32_e32 v51, 16, v31
	v_lshlrev_b32_e32 v50, 16, v27
	v_pk_mul_f32 v[52:53], v[50:51], v[46:47]
	v_pk_mul_f32 v[50:51], v[46:47], v[50:51] op_sel:[1,0] op_sel_hi:[0,1]
	v_sub_f32_e32 v48, v52, v53
	v_mul_f32_e32 v54, 0x3db504f3, v48
	v_add_f32_e32 v48, v50, v51
	v_lshlrev_b32_e32 v51, 16, v39
	v_lshlrev_b32_e32 v50, 16, v35
	v_pk_mul_f32 v[52:53], v[50:51], v[46:47]
	v_pk_mul_f32 v[46:47], v[46:47], v[50:51] op_sel:[1,0] op_sel_hi:[0,1]
	v_mul_f32_e32 v55, 0x3db504f3, v48
	v_sub_f32_e32 v52, v52, v53
	v_add_f32_e32 v53, v46, v47
	v_lshlrev_b32_e32 v46, 16, v49
	v_and_b32_e32 v47, 0xffff0000, v49
	v_and_b32_e32 v49, 0xffff0000, v31
	v_and_b32_e32 v48, 0xffff0000, v27
	v_pk_mul_f32 v[50:51], v[48:49], v[46:47]
	v_pk_mul_f32 v[48:49], v[46:47], v[48:49] op_sel:[1,0] op_sel_hi:[0,1]
	v_add_f32_e32 v31, v48, v49
	v_and_b32_e32 v49, 0xffff0000, v39
	v_and_b32_e32 v48, 0xffff0000, v35
	v_sub_f32_e32 v27, v50, v51
	v_pk_mul_f32 v[50:51], v[48:49], v[46:47]
	v_pk_mul_f32 v[46:47], v[46:47], v[48:49] op_sel:[1,0] op_sel_hi:[0,1]
	v_mul_f32_e32 v27, 0x3db504f3, v27
	v_mul_f32_e32 v31, 0x3db504f3, v31
	v_add_f32_e32 v46, v46, v47
	v_sub_f32_e32 v50, v50, v51
	v_cvt_pk_bf16_f32 v39, v54, v27
	v_cvt_pk_bf16_f32 v35, v55, v31
	v_cvt_pk_bf16_f32 v31, v52, v50
	v_cvt_pk_bf16_f32 v27, v53, v46
	v_lshlrev_b32_e32 v46, 16, v42
	v_and_b32_e32 v47, 0xffff0000, v42
	v_lshlrev_b32_e32 v49, 16, v32
	v_lshlrev_b32_e32 v48, 16, v28
	v_pk_mul_f32 v[50:51], v[48:49], v[46:47]
	v_pk_mul_f32 v[48:49], v[46:47], v[48:49] op_sel:[1,0] op_sel_hi:[0,1]
	v_sub_f32_e32 v42, v50, v51
	v_mul_f32_e32 v52, 0x3db504f3, v42
	v_add_f32_e32 v42, v48, v49
	v_lshlrev_b32_e32 v49, 16, v40
	v_lshlrev_b32_e32 v48, 16, v36
	v_pk_mul_f32 v[50:51], v[48:49], v[46:47]
	v_pk_mul_f32 v[46:47], v[46:47], v[48:49] op_sel:[1,0] op_sel_hi:[0,1]
	v_mul_f32_e32 v53, 0x3db504f3, v42
	v_sub_f32_e32 v50, v50, v51
	v_add_f32_e32 v51, v46, v47
	v_lshlrev_b32_e32 v42, 16, v43
	v_and_b32_e32 v43, 0xffff0000, v43
	v_and_b32_e32 v47, 0xffff0000, v32
	v_and_b32_e32 v46, 0xffff0000, v28
	v_pk_mul_f32 v[48:49], v[46:47], v[42:43]
	v_pk_mul_f32 v[46:47], v[42:43], v[46:47] op_sel:[1,0] op_sel_hi:[0,1]
	v_add_f32_e32 v32, v46, v47
	v_and_b32_e32 v47, 0xffff0000, v40
	v_and_b32_e32 v46, 0xffff0000, v36
	v_sub_f32_e32 v28, v48, v49
	v_pk_mul_f32 v[48:49], v[46:47], v[42:43]
	v_pk_mul_f32 v[42:43], v[42:43], v[46:47] op_sel:[1,0] op_sel_hi:[0,1]
	v_mul_f32_e32 v28, 0x3db504f3, v28
	v_mul_f32_e32 v32, 0x3db504f3, v32
	v_add_f32_e32 v42, v42, v43
	v_sub_f32_e32 v48, v48, v49
	v_cvt_pk_bf16_f32 v40, v52, v28
	v_cvt_pk_bf16_f32 v36, v53, v32
	v_cvt_pk_bf16_f32 v32, v50, v48
	v_cvt_pk_bf16_f32 v28, v51, v42
	v_and_b32_e32 v42, 0xffff0000, v44
	v_lshlrev_b32_e32 v43, 16, v44
	v_lshlrev_b32_e32 v47, 16, v41
	v_lshlrev_b32_e32 v46, 16, v37
	v_pk_mul_f32 v[48:49], v[46:47], v[42:43]
	v_pk_mul_f32 v[46:47], v[42:43], v[46:47] op_sel:[1,0] op_sel_hi:[0,1]
	v_add_f32_e32 v48, v48, v49
	v_sub_f32_e32 v49, v46, v47
	v_lshlrev_b32_e32 v47, 16, v33
	v_lshlrev_b32_e32 v46, 16, v29
	v_pk_mul_f32 v[50:51], v[46:47], v[42:43]
	v_pk_mul_f32 v[42:43], v[42:43], v[46:47] op_sel:[1,0] op_sel_hi:[0,1]
	v_add_f32_e32 v44, v50, v51
	v_mul_f32_e32 v50, 0x3db504f3, v44
	v_and_b32_e32 v44, 0xffff0000, v45
	v_lshlrev_b32_e32 v45, 16, v45
	v_and_b32_e32 v47, 0xffff0000, v33
	v_and_b32_e32 v46, 0xffff0000, v29
	v_sub_f32_e32 v42, v42, v43
	v_pk_mul_f32 v[52:53], v[44:45], v[46:47] op_sel:[1,0] op_sel_hi:[0,1]
	v_pk_mul_f32 v[46:47], v[46:47], v[44:45]
	v_mul_f32_e32 v51, 0x3db504f3, v42
	v_and_b32_e32 v43, 0xffff0000, v41
	v_and_b32_e32 v42, 0xffff0000, v37
	v_sub_f32_e32 v29, v52, v53
	v_add_f32_e32 v33, v46, v47
	v_mul_f32_e32 v29, 0x3db504f3, v29
	v_mul_f32_e32 v33, 0x3db504f3, v33
	v_pk_mul_f32 v[46:47], v[44:45], v[42:43] op_sel:[1,0] op_sel_hi:[0,1]
	v_pk_mul_f32 v[42:43], v[42:43], v[44:45]
	v_cvt_pk_bf16_f32 v41, v51, v29
	v_sub_f32_e32 v46, v46, v47
	v_add_f32_e32 v42, v42, v43
	v_cvt_pk_bf16_f32 v37, v50, v33
	v_cvt_pk_bf16_f32 v33, v49, v46
	v_cvt_pk_bf16_f32 v29, v48, v42
	ds_write_b128 v161, v[38:41] offset:16
	ds_write_b128 v161, v[34:37] offset:144
	ds_write_b128 v161, v[30:33] offset:34832
	ds_write_b128 v161, v[26:29] offset:34960
	s_cbranch_scc1 .LBB0_314
	s_add_i32 s93, s93, s3
	s_cmpk_lt_i32 s93, 0x80
	s_waitcnt lgkmcnt(0)
	s_barrier
	s_cbranch_scc1 .LBB0_311
